# write-through (sc1) stores in the two small opening phases and no L2 writeback at their barriers
# baseline (speedup 1.0000x reference)
; DI float rdlane(float v, int l) { return __uint_as_float((unsigned)__builtin_amdgcn_readlane((int)__float_as_uint(v), l)); }
; DI void ph_adaln(const float* cnd, const float* cctx, const float* ada_w, float* modp, int gw, int NGW, int lane) {
;     ...
;             for (int kk = 0; kk < 64; ++kk) {
;                 const f32x4 w = __builtin_nontemporal_load((const f32x4*)(wp + (size_t)(hh * 64 + kk) * NMOD));
; #pragma unroll
;                 for (int r = 0; r < 9; ++r) { const float s = rdlane(sv[r][hh], kk); acc[r] += w * s; }
.LBB0_11:
	v_add_co_u32_e64 v62, s[6:7], s11, v42
	s_mov_b32 s2, 0xfff58000
	s_nop 0
	v_addc_co_u32_e64 v63, s[6:7], -1, v43, s[6:7]
	v_add_co_u32_e64 v64, s[6:7], s13, v42
	v_add_co_u32_e32 v44, vcc, 0xfff4c000, v42
	s_nop 0
	v_addc_co_u32_e64 v65, s[6:7], -1, v43, s[6:7]
	v_add_co_u32_e64 v60, s[6:7], s17, v42
	v_addc_co_u32_e32 v45, vcc, -1, v43, vcc
	s_nop 0
	v_addc_co_u32_e64 v61, s[6:7], -1, v43, s[6:7]
	v_add_co_u32_e64 v58, s[6:7], s19, v42
	global_load_dwordx4 v[38:41], v[42:43], off nt
	s_nop 0
	v_addc_co_u32_e64 v59, s[6:7], -1, v43, s[6:7]
	v_add_co_u32_e64 v56, s[6:7], s21, v42
	s_mov_b32 s4, 0xfff64000
	s_nop 0
	v_addc_co_u32_e64 v57, s[6:7], -1, v43, s[6:7]
	v_add_co_u32_e64 v54, s[6:7], s23, v42
	s_mov_b32 s8, 0xfff70000
	s_nop 0
	v_addc_co_u32_e64 v55, s[6:7], -1, v43, s[6:7]
	v_add_co_u32_e64 v48, s[6:7], s25, v42
	s_mov_b32 s10, 0xfff7c000
	s_nop 0
	v_addc_co_u32_e64 v49, s[6:7], -1, v43, s[6:7]
	v_add_co_u32_e64 v46, s[6:7], s27, v42
	v_readlane_b32 s16, v50, s35
	s_nop 0
	v_addc_co_u32_e64 v47, s[6:7], -1, v43, s[6:7]
	v_add_co_u32_e64 v88, s[6:7], s2, v42
	v_readlane_b32 s18, v74, s35
	s_nop 0
	v_addc_co_u32_e64 v89, s[6:7], -1, v43, s[6:7]
	global_load_dwordx4 v[84:87], v[44:45], off nt
	s_nop 0
	global_load_dwordx4 v[88:91], v[88:89], off nt
	v_add_co_u32_e64 v92, s[6:7], s4, v42
	v_readlane_b32 s20, v75, s35
	s_nop 0
	v_addc_co_u32_e64 v93, s[6:7], -1, v43, s[6:7]
	v_add_co_u32_e64 v72, s[6:7], s8, v42
	v_readlane_b32 s22, v76, s35
	s_nop 0
	v_addc_co_u32_e64 v73, s[6:7], -1, v43, s[6:7]
	v_add_co_u32_e64 v70, s[6:7], s10, v42
	v_readlane_b32 s24, v77, s35
	v_readlane_b32 s26, v78, s35
	v_readlane_b32 s28, v79, s35
	v_readlane_b32 s30, v81, s35
	v_readlane_b32 s36, v82, s35
	s_add_i32 s0, s35, 1
	s_mov_b32 s12, 0xfff88000
	s_add_i32 s37, s35, 13
	v_addc_co_u32_e64 v71, s[6:7], -1, v43, s[6:7]
	s_add_i32 s43, s35, 12
	v_add_co_u32_e64 v68, s[6:7], s12, v42
	v_readlane_b32 s68, v50, s0
	v_readlane_b32 s70, v74, s0
	v_readlane_b32 s2, v75, s0
	v_readlane_b32 s12, v76, s0
	v_readlane_b32 s88, v77, s0
	v_readlane_b32 s86, v78, s0
	v_readlane_b32 s42, v79, s0
	v_readlane_b32 s10, v81, s0
	v_readlane_b32 s62, v82, s0
	s_add_i32 s40, s35, 2
	s_mov_b32 s34, 0xfff94000
	v_addc_co_u32_e64 v69, s[6:7], -1, v43, s[6:7]
	s_add_i32 s38, s35, 3
	s_add_i32 s48, s35, 4
	s_add_i32 s57, s35, 5
	s_add_i32 s55, s35, 6
	s_add_i32 s53, s35, 7
	s_add_i32 s51, s35, 8
	s_add_i32 s49, s35, 9
	s_add_i32 s47, s35, 10
	s_add_i32 s45, s35, 11
	s_add_i32 s41, s35, 14
	s_add_i32 s39, s35, 15
	s_add_i32 s35, s35, 16
	v_add_co_u32_e64 v66, s[6:7], s34, v42
	v_readlane_b32 s66, v50, s40
	v_readlane_b32 s84, v74, s40
	v_readlane_b32 s78, v75, s40
	v_readlane_b32 s8, v76, s40
	v_readlane_b32 s4, v77, s40
	v_readlane_b32 s34, v78, s40
	v_readlane_b32 s60, v79, s40
	v_readlane_b32 s56, v81, s40
	v_readlane_b32 s58, v82, s40
	v_readlane_b32 s64, v50, s38
	v_readlane_b32 s72, v74, s38
	v_readlane_b32 s74, v75, s38
	v_readlane_b32 s76, v76, s38
	v_readlane_b32 s54, v77, s38
	v_readlane_b32 s52, v78, s38
	v_readlane_b32 s50, v79, s38
	v_readlane_b32 s46, v81, s38
	v_readlane_b32 s44, v82, s38
	v_addc_co_u32_e64 v67, s[6:7], -1, v43, s[6:7]
	v_readlane_b32 s6, v50, s48
	v_readlane_b32 s38, v78, s48
	v_readlane_b32 s40, v79, s48
	v_readlane_b32 s0, v81, s48
	v_readlane_b32 s94, v75, s55
	v_readlane_b32 s96, v76, s55
	s_waitcnt vmcnt(1)
	v_pk_fma_f32 v[34:35], v[84:85], s[16:17], v[34:35] op_sel_hi:[1,0,1]
	v_pk_fma_f32 v[30:31], v[84:85], s[18:19], v[30:31] op_sel_hi:[1,0,1]
	v_pk_fma_f32 v[26:27], v[84:85], s[20:21], v[26:27] op_sel_hi:[1,0,1]
	v_pk_fma_f32 v[22:23], v[84:85], s[22:23], v[22:23] op_sel_hi:[1,0,1]
	v_pk_fma_f32 v[18:19], v[84:85], s[24:25], v[18:19] op_sel_hi:[1,0,1]
	v_pk_fma_f32 v[14:15], v[84:85], s[26:27], v[14:15] op_sel_hi:[1,0,1]
	v_pk_fma_f32 v[10:11], v[84:85], s[28:29], v[10:11] op_sel_hi:[1,0,1]
	v_pk_fma_f32 v[8:9], v[86:87], s[30:31], v[8:9] op_sel_hi:[1,0,1]
	v_pk_fma_f32 v[6:7], v[84:85], s[30:31], v[6:7] op_sel_hi:[1,0,1]
	v_pk_fma_f32 v[4:5], v[86:87], s[36:37], v[4:5] op_sel_hi:[1,0,1]
	v_pk_fma_f32 v[2:3], v[84:85], s[36:37], v[2:3] op_sel_hi:[1,0,1]
	v_pk_fma_f32 v[36:37], v[86:87], s[16:17], v[36:37] op_sel_hi:[1,0,1]
	v_pk_fma_f32 v[32:33], v[86:87], s[18:19], v[32:33] op_sel_hi:[1,0,1]
	v_pk_fma_f32 v[28:29], v[86:87], s[20:21], v[28:29] op_sel_hi:[1,0,1]
	v_pk_fma_f32 v[24:25], v[86:87], s[22:23], v[24:25] op_sel_hi:[1,0,1]
	v_pk_fma_f32 v[20:21], v[86:87], s[24:25], v[20:21] op_sel_hi:[1,0,1]
	v_pk_fma_f32 v[16:17], v[86:87], s[26:27], v[16:17] op_sel_hi:[1,0,1]
	v_pk_fma_f32 v[12:13], v[86:87], s[28:29], v[12:13] op_sel_hi:[1,0,1]
	s_waitcnt vmcnt(0)
; DI float rdlane(float v, int l) { return __uint_as_float((unsigned)__builtin_amdgcn_readlane((int)__float_as_uint(v), l)); }
; DI void ph_adaln(const float* cnd, const float* cctx, const float* ada_w, float* modp, int gw, int NGW, int lane) {
;     ...
;             for (int kk = 0; kk < 64; ++kk) {
;                 const f32x4 w = __builtin_nontemporal_load((const f32x4*)(wp + (size_t)(hh * 64 + kk) * NMOD));
; #pragma unroll
;                 for (int r = 0; r < 9; ++r) { const float s = rdlane(sv[r][hh], kk); acc[r] += w * s; }
	v_pk_fma_f32 v[34:35], v[88:89], s[68:69], v[34:35] op_sel_hi:[1,0,1]
	v_pk_fma_f32 v[30:31], v[88:89], s[70:71], v[30:31] op_sel_hi:[1,0,1]
	v_pk_fma_f32 v[26:27], v[88:89], s[2:3], v[26:27] op_sel_hi:[1,0,1]
	v_pk_fma_f32 v[22:23], v[88:89], s[12:13], v[22:23] op_sel_hi:[1,0,1]
	v_pk_fma_f32 v[18:19], v[88:89], s[88:89], v[18:19] op_sel_hi:[1,0,1]
	v_pk_fma_f32 v[14:15], v[88:89], s[86:87], v[14:15] op_sel_hi:[1,0,1]
	v_pk_fma_f32 v[10:11], v[88:89], s[42:43], v[10:11] op_sel_hi:[1,0,1]
	v_pk_fma_f32 v[44:45], v[90:91], s[10:11], v[8:9] op_sel_hi:[1,0,1]
	v_pk_fma_f32 v[84:85], v[88:89], s[10:11], v[6:7] op_sel_hi:[1,0,1]
	v_pk_fma_f32 v[86:87], v[90:91], s[62:63], v[4:5] op_sel_hi:[1,0,1]
	v_pk_fma_f32 v[88:89], v[88:89], s[62:63], v[2:3] op_sel_hi:[1,0,1]
	global_load_dwordx4 v[2:5], v[92:93], off nt
	global_load_dwordx4 v[6:9], v[72:73], off nt
	v_pk_fma_f32 v[36:37], v[90:91], s[68:69], v[36:37] op_sel_hi:[1,0,1]
	v_pk_fma_f32 v[32:33], v[90:91], s[70:71], v[32:33] op_sel_hi:[1,0,1]
	v_pk_fma_f32 v[28:29], v[90:91], s[2:3], v[28:29] op_sel_hi:[1,0,1]
	v_pk_fma_f32 v[24:25], v[90:91], s[12:13], v[24:25] op_sel_hi:[1,0,1]
	v_pk_fma_f32 v[20:21], v[90:91], s[88:89], v[20:21] op_sel_hi:[1,0,1]
	v_pk_fma_f32 v[16:17], v[90:91], s[86:87], v[16:17] op_sel_hi:[1,0,1]
	v_pk_fma_f32 v[12:13], v[90:91], s[42:43], v[12:13] op_sel_hi:[1,0,1]
	v_readlane_b32 s16, v74, s48
	v_readlane_b32 s18, v75, s48
	v_readlane_b32 s20, v76, s48
	v_readlane_b32 s22, v77, s48
	v_readlane_b32 s48, v82, s48
	v_readlane_b32 s68, v50, s57
	v_readlane_b32 s70, v74, s57
	v_readlane_b32 s2, v75, s57
	v_readlane_b32 s12, v76, s57
	v_readlane_b32 s30, v77, s57
	v_readlane_b32 s36, v78, s57
	v_readlane_b32 s28, v79, s57
	v_readlane_b32 s42, v81, s57
	v_readlane_b32 s10, v82, s57
	v_readlane_b32 s62, v50, s55
	v_readlane_b32 s24, v75, s53
	v_readlane_b32 s26, v76, s53
	v_readlane_b32 s86, v81, s53
	v_readlane_b32 s88, v82, s53
	v_readlane_b32 s90, v50, s51
	v_readlane_b32 s92, v74, s51
	s_cmp_lg_u32 s35, 64
	v_lshl_add_u64 v[42:43], v[42:43], 0, s[14:15]
	s_waitcnt vmcnt(1)
	v_pk_fma_f32 v[36:37], v[4:5], s[66:67], v[36:37] op_sel_hi:[1,0,1]
	v_pk_fma_f32 v[34:35], v[2:3], s[66:67], v[34:35] op_sel_hi:[1,0,1]
	v_pk_fma_f32 v[32:33], v[4:5], s[84:85], v[32:33] op_sel_hi:[1,0,1]
	v_pk_fma_f32 v[30:31], v[2:3], s[84:85], v[30:31] op_sel_hi:[1,0,1]
	v_pk_fma_f32 v[28:29], v[4:5], s[78:79], v[28:29] op_sel_hi:[1,0,1]
	v_pk_fma_f32 v[26:27], v[2:3], s[78:79], v[26:27] op_sel_hi:[1,0,1]
	v_pk_fma_f32 v[24:25], v[4:5], s[8:9], v[24:25] op_sel_hi:[1,0,1]
	v_pk_fma_f32 v[22:23], v[2:3], s[8:9], v[22:23] op_sel_hi:[1,0,1]
	v_pk_fma_f32 v[20:21], v[4:5], s[4:5], v[20:21] op_sel_hi:[1,0,1]
	v_pk_fma_f32 v[18:19], v[2:3], s[4:5], v[18:19] op_sel_hi:[1,0,1]
	v_pk_fma_f32 v[16:17], v[4:5], s[34:35], v[16:17] op_sel_hi:[1,0,1]
	v_pk_fma_f32 v[14:15], v[2:3], s[34:35], v[14:15] op_sel_hi:[1,0,1]
	v_pk_fma_f32 v[12:13], v[4:5], s[60:61], v[12:13] op_sel_hi:[1,0,1]
	v_pk_fma_f32 v[10:11], v[2:3], s[60:61], v[10:11] op_sel_hi:[1,0,1]
	v_pk_fma_f32 v[44:45], v[4:5], s[56:57], v[44:45] op_sel_hi:[1,0,1]
	v_pk_fma_f32 v[72:73], v[2:3], s[56:57], v[84:85] op_sel_hi:[1,0,1]
	v_pk_fma_f32 v[4:5], v[4:5], s[58:59], v[86:87] op_sel_hi:[1,0,1]
	v_pk_fma_f32 v[2:3], v[2:3], s[58:59], v[88:89] op_sel_hi:[1,0,1]
	s_waitcnt vmcnt(0)
	v_pk_fma_f32 v[36:37], v[8:9], s[64:65], v[36:37] op_sel_hi:[1,0,1]
	v_pk_fma_f32 v[34:35], v[6:7], s[64:65], v[34:35] op_sel_hi:[1,0,1]
	v_pk_fma_f32 v[32:33], v[8:9], s[72:73], v[32:33] op_sel_hi:[1,0,1]
	v_pk_fma_f32 v[30:31], v[6:7], s[72:73], v[30:31] op_sel_hi:[1,0,1]
	v_pk_fma_f32 v[28:29], v[8:9], s[74:75], v[28:29] op_sel_hi:[1,0,1]
	v_pk_fma_f32 v[26:27], v[6:7], s[74:75], v[26:27] op_sel_hi:[1,0,1]
	v_pk_fma_f32 v[24:25], v[8:9], s[76:77], v[24:25] op_sel_hi:[1,0,1]
	v_pk_fma_f32 v[22:23], v[6:7], s[76:77], v[22:23] op_sel_hi:[1,0,1]
	v_pk_fma_f32 v[20:21], v[8:9], s[54:55], v[20:21] op_sel_hi:[1,0,1]
	v_pk_fma_f32 v[18:19], v[6:7], s[54:55], v[18:19] op_sel_hi:[1,0,1]
	v_pk_fma_f32 v[16:17], v[8:9], s[52:53], v[16:17] op_sel_hi:[1,0,1]
	v_pk_fma_f32 v[14:15], v[6:7], s[52:53], v[14:15] op_sel_hi:[1,0,1]
	v_pk_fma_f32 v[12:13], v[8:9], s[50:51], v[12:13] op_sel_hi:[1,0,1]
	v_pk_fma_f32 v[10:11], v[6:7], s[50:51], v[10:11] op_sel_hi:[1,0,1]
	v_pk_fma_f32 v[44:45], v[8:9], s[46:47], v[44:45] op_sel_hi:[1,0,1]
	v_pk_fma_f32 v[72:73], v[6:7], s[46:47], v[72:73] op_sel_hi:[1,0,1]
	v_pk_fma_f32 v[84:85], v[8:9], s[44:45], v[4:5] op_sel_hi:[1,0,1]
	v_pk_fma_f32 v[86:87], v[6:7], s[44:45], v[2:3] op_sel_hi:[1,0,1]
	global_load_dwordx4 v[2:5], v[70:71], off nt
	global_load_dwordx4 v[6:9], v[68:69], off nt
	v_readlane_b32 s66, v74, s55
	v_readlane_b32 s8, v77, s55
	v_readlane_b32 s4, v78, s55
	v_readlane_b32 s34, v79, s55
	v_readlane_b32 s84, v81, s55
	v_readlane_b32 s56, v82, s55
	v_readlane_b32 s58, v50, s53
	v_readlane_b32 s60, v74, s53
	v_readlane_b32 s74, v77, s53
	v_readlane_b32 s76, v78, s53
	v_readlane_b32 s78, v79, s53
	v_readlane_b32 s44, v75, s51
	v_readlane_b32 s46, v76, s51
	v_readlane_b32 s50, v77, s51
	v_readlane_b32 s52, v78, s51
	v_readlane_b32 s54, v79, s51
	v_readlane_b32 s64, v81, s51
	v_readlane_b32 s72, v82, s51
	s_waitcnt vmcnt(1)
; DI float rdlane(float v, int l) { return __uint_as_float((unsigned)__builtin_amdgcn_readlane((int)__float_as_uint(v), l)); }
; DI void ph_adaln(const float* cnd, const float* cctx, const float* ada_w, float* modp, int gw, int NGW, int lane) {
;     ...
;             for (int kk = 0; kk < 64; ++kk) {
;                 const f32x4 w = __builtin_nontemporal_load((const f32x4*)(wp + (size_t)(hh * 64 + kk) * NMOD));
; #pragma unroll
;                 for (int r = 0; r < 9; ++r) { const float s = rdlane(sv[r][hh], kk); acc[r] += w * s; }
	v_pk_fma_f32 v[36:37], v[4:5], s[6:7], v[36:37] op_sel_hi:[1,0,1]
	v_pk_fma_f32 v[34:35], v[2:3], s[6:7], v[34:35] op_sel_hi:[1,0,1]
	v_pk_fma_f32 v[32:33], v[4:5], s[16:17], v[32:33] op_sel_hi:[1,0,1]
	v_pk_fma_f32 v[30:31], v[2:3], s[16:17], v[30:31] op_sel_hi:[1,0,1]
	v_pk_fma_f32 v[28:29], v[4:5], s[18:19], v[28:29] op_sel_hi:[1,0,1]
	v_pk_fma_f32 v[26:27], v[2:3], s[18:19], v[26:27] op_sel_hi:[1,0,1]
	v_pk_fma_f32 v[24:25], v[4:5], s[20:21], v[24:25] op_sel_hi:[1,0,1]
	v_pk_fma_f32 v[22:23], v[2:3], s[20:21], v[22:23] op_sel_hi:[1,0,1]
	v_pk_fma_f32 v[20:21], v[4:5], s[22:23], v[20:21] op_sel_hi:[1,0,1]
	v_pk_fma_f32 v[68:69], v[2:3], s[22:23], v[18:19] op_sel_hi:[1,0,1]
	v_pk_fma_f32 v[70:71], v[4:5], s[38:39], v[16:17] op_sel_hi:[1,0,1]
	v_pk_fma_f32 v[88:89], v[2:3], s[38:39], v[14:15] op_sel_hi:[1,0,1]
	v_pk_fma_f32 v[90:91], v[4:5], s[40:41], v[12:13] op_sel_hi:[1,0,1]
	v_pk_fma_f32 v[92:93], v[2:3], s[40:41], v[10:11] op_sel_hi:[1,0,1]
	v_pk_fma_f32 v[44:45], v[4:5], s[0:1], v[44:45] op_sel_hi:[1,0,1]
	v_pk_fma_f32 v[72:73], v[2:3], s[0:1], v[72:73] op_sel_hi:[1,0,1]
	v_pk_fma_f32 v[4:5], v[4:5], s[48:49], v[84:85] op_sel_hi:[1,0,1]
	v_pk_fma_f32 v[2:3], v[2:3], s[48:49], v[86:87] op_sel_hi:[1,0,1]
	s_waitcnt vmcnt(0)
	v_pk_fma_f32 v[84:85], v[8:9], s[68:69], v[36:37] op_sel_hi:[1,0,1]
	v_pk_fma_f32 v[86:87], v[6:7], s[68:69], v[34:35] op_sel_hi:[1,0,1]
	v_pk_fma_f32 v[94:95], v[8:9], s[70:71], v[32:33] op_sel_hi:[1,0,1]
	v_pk_fma_f32 v[96:97], v[6:7], s[70:71], v[30:31] op_sel_hi:[1,0,1]
	v_pk_fma_f32 v[10:11], v[8:9], s[2:3], v[28:29] op_sel_hi:[1,0,1]
	v_pk_fma_f32 v[12:13], v[6:7], s[2:3], v[26:27] op_sel_hi:[1,0,1]
	v_pk_fma_f32 v[14:15], v[8:9], s[12:13], v[24:25] op_sel_hi:[1,0,1]
	v_pk_fma_f32 v[16:17], v[6:7], s[12:13], v[22:23] op_sel_hi:[1,0,1]
	v_pk_fma_f32 v[18:19], v[8:9], s[30:31], v[20:21] op_sel_hi:[1,0,1]
	v_pk_fma_f32 v[20:21], v[6:7], s[30:31], v[68:69] op_sel_hi:[1,0,1]
	v_pk_fma_f32 v[22:23], v[8:9], s[36:37], v[70:71] op_sel_hi:[1,0,1]
	v_pk_fma_f32 v[24:25], v[6:7], s[36:37], v[88:89] op_sel_hi:[1,0,1]
	v_pk_fma_f32 v[26:27], v[8:9], s[28:29], v[90:91] op_sel_hi:[1,0,1]
	v_pk_fma_f32 v[28:29], v[6:7], s[28:29], v[92:93] op_sel_hi:[1,0,1]
	v_pk_fma_f32 v[30:31], v[8:9], s[42:43], v[44:45] op_sel_hi:[1,0,1]
	v_pk_fma_f32 v[32:33], v[6:7], s[42:43], v[72:73] op_sel_hi:[1,0,1]
	v_pk_fma_f32 v[34:35], v[8:9], s[10:11], v[4:5] op_sel_hi:[1,0,1]
	v_pk_fma_f32 v[36:37], v[6:7], s[10:11], v[2:3] op_sel_hi:[1,0,1]
	global_load_dwordx4 v[6:9], v[64:65], off nt
	s_nop 0
	global_load_dwordx4 v[64:67], v[66:67], off nt
	s_nop 0
	global_load_dwordx4 v[68:71], v[62:63], off nt
	global_load_dwordx4 v[2:5], v[60:61], off nt
	v_readlane_b32 s6, v50, s49
	v_readlane_b32 s16, v74, s49
	v_readlane_b32 s20, v76, s49
	v_readlane_b32 s22, v77, s49
	v_readlane_b32 s18, v75, s49
	v_readlane_b32 s48, v78, s49
	v_readlane_b32 s30, v79, s49
	v_readlane_b32 s36, v81, s49
	v_readlane_b32 s38, v82, s49
	v_readlane_b32 s40, v50, s47
	v_readlane_b32 s42, v74, s47
	v_readlane_b32 s28, v75, s47
	v_readlane_b32 s68, v78, s47
	v_readlane_b32 s70, v79, s47
	v_readlane_b32 s10, v50, s45
	v_readlane_b32 s12, v81, s45
	v_readlane_b32 s0, v74, s43
	v_readlane_b32 s2, v75, s43
	s_waitcnt vmcnt(2)
	v_pk_fma_f32 v[44:45], v[66:67], s[62:63], v[84:85] op_sel_hi:[1,0,1]
	v_pk_fma_f32 v[62:63], v[64:65], s[62:63], v[86:87] op_sel_hi:[1,0,1]
	v_pk_fma_f32 v[72:73], v[66:67], s[66:67], v[94:95] op_sel_hi:[1,0,1]
	v_pk_fma_f32 v[84:85], v[64:65], s[66:67], v[96:97] op_sel_hi:[1,0,1]
	v_pk_fma_f32 v[60:61], v[66:67], s[94:95], v[10:11] op_sel_hi:[1,0,1]
	v_pk_fma_f32 v[86:87], v[64:65], s[94:95], v[12:13] op_sel_hi:[1,0,1]
	v_pk_fma_f32 v[14:15], v[66:67], s[96:97], v[14:15] op_sel_hi:[1,0,1]
	v_pk_fma_f32 v[16:17], v[64:65], s[96:97], v[16:17] op_sel_hi:[1,0,1]
	v_pk_fma_f32 v[18:19], v[66:67], s[8:9], v[18:19] op_sel_hi:[1,0,1]
	v_pk_fma_f32 v[20:21], v[64:65], s[8:9], v[20:21] op_sel_hi:[1,0,1]
	v_pk_fma_f32 v[22:23], v[66:67], s[4:5], v[22:23] op_sel_hi:[1,0,1]
	v_pk_fma_f32 v[24:25], v[64:65], s[4:5], v[24:25] op_sel_hi:[1,0,1]
	v_pk_fma_f32 v[26:27], v[66:67], s[34:35], v[26:27] op_sel_hi:[1,0,1]
	v_pk_fma_f32 v[28:29], v[64:65], s[34:35], v[28:29] op_sel_hi:[1,0,1]
	v_pk_fma_f32 v[30:31], v[66:67], s[84:85], v[30:31] op_sel_hi:[1,0,1]
	v_pk_fma_f32 v[32:33], v[64:65], s[84:85], v[32:33] op_sel_hi:[1,0,1]
	v_pk_fma_f32 v[34:35], v[66:67], s[56:57], v[34:35] op_sel_hi:[1,0,1]
	v_pk_fma_f32 v[36:37], v[64:65], s[56:57], v[36:37] op_sel_hi:[1,0,1]
	global_load_dwordx4 v[10:13], v[58:59], off nt
	s_waitcnt vmcnt(2)
; DI float rdlane(float v, int l) { return __uint_as_float((unsigned)__builtin_amdgcn_readlane((int)__float_as_uint(v), l)); }
; DI void ph_adaln(const float* cnd, const float* cctx, const float* ada_w, float* modp, int gw, int NGW, int lane) {
;     ...
;             for (int kk = 0; kk < 64; ++kk) {
;                 const f32x4 w = __builtin_nontemporal_load((const f32x4*)(wp + (size_t)(hh * 64 + kk) * NMOD));
; #pragma unroll
;                 for (int r = 0; r < 9; ++r) { const float s = rdlane(sv[r][hh], kk); acc[r] += w * s; }
	v_pk_fma_f32 v[44:45], v[70:71], s[58:59], v[44:45] op_sel_hi:[1,0,1]
	v_pk_fma_f32 v[62:63], v[68:69], s[58:59], v[62:63] op_sel_hi:[1,0,1]
	v_pk_fma_f32 v[64:65], v[70:71], s[60:61], v[72:73] op_sel_hi:[1,0,1]
	v_pk_fma_f32 v[66:67], v[68:69], s[60:61], v[84:85] op_sel_hi:[1,0,1]
	v_pk_fma_f32 v[72:73], v[70:71], s[26:27], v[14:15] op_sel_hi:[1,0,1]
	v_pk_fma_f32 v[84:85], v[68:69], s[26:27], v[16:17] op_sel_hi:[1,0,1]
	v_pk_fma_f32 v[18:19], v[70:71], s[74:75], v[18:19] op_sel_hi:[1,0,1]
	v_pk_fma_f32 v[20:21], v[68:69], s[74:75], v[20:21] op_sel_hi:[1,0,1]
	v_pk_fma_f32 v[22:23], v[70:71], s[76:77], v[22:23] op_sel_hi:[1,0,1]
	v_pk_fma_f32 v[24:25], v[68:69], s[76:77], v[24:25] op_sel_hi:[1,0,1]
	v_pk_fma_f32 v[26:27], v[70:71], s[78:79], v[26:27] op_sel_hi:[1,0,1]
	v_pk_fma_f32 v[28:29], v[68:69], s[78:79], v[28:29] op_sel_hi:[1,0,1]
	v_pk_fma_f32 v[30:31], v[70:71], s[86:87], v[30:31] op_sel_hi:[1,0,1]
	v_pk_fma_f32 v[32:33], v[68:69], s[86:87], v[32:33] op_sel_hi:[1,0,1]
	v_pk_fma_f32 v[34:35], v[70:71], s[88:89], v[34:35] op_sel_hi:[1,0,1]
	v_pk_fma_f32 v[36:37], v[68:69], s[88:89], v[36:37] op_sel_hi:[1,0,1]
	global_load_dwordx4 v[14:17], v[56:57], off nt
	v_pk_fma_f32 v[58:59], v[70:71], s[24:25], v[60:61] op_sel_hi:[1,0,1]
	v_pk_fma_f32 v[60:61], v[68:69], s[24:25], v[86:87] op_sel_hi:[1,0,1]
	v_pk_fma_f32 v[44:45], v[8:9], s[90:91], v[44:45] op_sel_hi:[1,0,1]
	v_pk_fma_f32 v[62:63], v[6:7], s[90:91], v[62:63] op_sel_hi:[1,0,1]
	v_pk_fma_f32 v[64:65], v[8:9], s[92:93], v[64:65] op_sel_hi:[1,0,1]
	v_pk_fma_f32 v[66:67], v[6:7], s[92:93], v[66:67] op_sel_hi:[1,0,1]
	v_pk_fma_f32 v[56:57], v[8:9], s[44:45], v[58:59] op_sel_hi:[1,0,1]
	v_pk_fma_f32 v[58:59], v[6:7], s[44:45], v[60:61] op_sel_hi:[1,0,1]
	v_pk_fma_f32 v[60:61], v[8:9], s[46:47], v[72:73] op_sel_hi:[1,0,1]
	v_pk_fma_f32 v[68:69], v[6:7], s[46:47], v[84:85] op_sel_hi:[1,0,1]
	v_pk_fma_f32 v[18:19], v[8:9], s[50:51], v[18:19] op_sel_hi:[1,0,1]
	v_pk_fma_f32 v[20:21], v[6:7], s[50:51], v[20:21] op_sel_hi:[1,0,1]
	v_pk_fma_f32 v[22:23], v[8:9], s[52:53], v[22:23] op_sel_hi:[1,0,1]
	v_pk_fma_f32 v[24:25], v[6:7], s[52:53], v[24:25] op_sel_hi:[1,0,1]
	v_pk_fma_f32 v[26:27], v[8:9], s[54:55], v[26:27] op_sel_hi:[1,0,1]
	v_pk_fma_f32 v[28:29], v[6:7], s[54:55], v[28:29] op_sel_hi:[1,0,1]
	v_pk_fma_f32 v[30:31], v[8:9], s[64:65], v[30:31] op_sel_hi:[1,0,1]
	v_pk_fma_f32 v[32:33], v[6:7], s[64:65], v[32:33] op_sel_hi:[1,0,1]
	v_pk_fma_f32 v[34:35], v[8:9], s[72:73], v[34:35] op_sel_hi:[1,0,1]
	v_pk_fma_f32 v[36:37], v[6:7], s[72:73], v[36:37] op_sel_hi:[1,0,1]
	global_load_dwordx4 v[6:9], v[54:55], off nt
	s_waitcnt vmcnt(3)
	v_pk_fma_f32 v[54:55], v[2:3], s[6:7], v[62:63] op_sel_hi:[1,0,1]
	v_pk_fma_f32 v[62:63], v[4:5], s[16:17], v[64:65] op_sel_hi:[1,0,1]
	v_pk_fma_f32 v[64:65], v[2:3], s[16:17], v[66:67] op_sel_hi:[1,0,1]
	v_pk_fma_f32 v[66:67], v[2:3], s[20:21], v[68:69] op_sel_hi:[1,0,1]
	v_pk_fma_f32 v[68:69], v[4:5], s[22:23], v[18:19] op_sel_hi:[1,0,1]
	v_pk_fma_f32 v[70:71], v[2:3], s[22:23], v[20:21] op_sel_hi:[1,0,1]
	global_load_dwordx4 v[18:21], v[48:49], off nt
	v_pk_fma_f32 v[44:45], v[4:5], s[6:7], v[44:45] op_sel_hi:[1,0,1]
	v_pk_fma_f32 v[56:57], v[4:5], s[18:19], v[56:57] op_sel_hi:[1,0,1]
	v_pk_fma_f32 v[58:59], v[2:3], s[18:19], v[58:59] op_sel_hi:[1,0,1]
	v_pk_fma_f32 v[60:61], v[4:5], s[20:21], v[60:61] op_sel_hi:[1,0,1]
	v_pk_fma_f32 v[22:23], v[4:5], s[48:49], v[22:23] op_sel_hi:[1,0,1]
	v_pk_fma_f32 v[24:25], v[2:3], s[48:49], v[24:25] op_sel_hi:[1,0,1]
	v_pk_fma_f32 v[26:27], v[4:5], s[30:31], v[26:27] op_sel_hi:[1,0,1]
	v_pk_fma_f32 v[28:29], v[2:3], s[30:31], v[28:29] op_sel_hi:[1,0,1]
	v_pk_fma_f32 v[30:31], v[4:5], s[36:37], v[30:31] op_sel_hi:[1,0,1]
	v_pk_fma_f32 v[32:33], v[2:3], s[36:37], v[32:33] op_sel_hi:[1,0,1]
	v_pk_fma_f32 v[34:35], v[4:5], s[38:39], v[34:35] op_sel_hi:[1,0,1]
	v_pk_fma_f32 v[36:37], v[2:3], s[38:39], v[36:37] op_sel_hi:[1,0,1]
	global_load_dwordx4 v[2:5], v[46:47], off nt
	v_readlane_b32 s62, v76, s47
	v_readlane_b32 s66, v77, s47
	v_readlane_b32 s94, v81, s47
	v_readlane_b32 s96, v82, s47
	v_readlane_b32 s84, v74, s45
	v_readlane_b32 s34, v75, s45
	v_readlane_b32 s4, v76, s45
	v_readlane_b32 s8, v77, s45
	v_readlane_b32 s58, v78, s45
	v_readlane_b32 s60, v79, s45
	v_readlane_b32 s74, v82, s45
	v_readlane_b32 s76, v50, s43
	v_readlane_b32 s24, v76, s43
	v_readlane_b32 s26, v77, s43
	v_readlane_b32 s56, v78, s43
	v_readlane_b32 s44, v79, s43
	v_readlane_b32 s46, v81, s43
	v_readlane_b32 s50, v82, s43
	v_readlane_b32 s52, v50, s37
	v_readlane_b32 s54, v74, s37
	v_readlane_b32 s64, v75, s37
	s_waitcnt vmcnt(4)
	v_pk_fma_f32 v[44:45], v[12:13], s[40:41], v[44:45] op_sel_hi:[1,0,1]
	v_pk_fma_f32 v[48:49], v[10:11], s[40:41], v[54:55] op_sel_hi:[1,0,1]
	v_pk_fma_f32 v[54:55], v[12:13], s[42:43], v[62:63] op_sel_hi:[1,0,1]
	v_pk_fma_f32 v[62:63], v[10:11], s[42:43], v[64:65] op_sel_hi:[1,0,1]
	v_pk_fma_f32 v[46:47], v[12:13], s[28:29], v[56:57] op_sel_hi:[1,0,1]
	v_pk_fma_f32 v[56:57], v[10:11], s[28:29], v[58:59] op_sel_hi:[1,0,1]
	v_pk_fma_f32 v[58:59], v[12:13], s[62:63], v[60:61] op_sel_hi:[1,0,1]
	v_pk_fma_f32 v[60:61], v[10:11], s[62:63], v[66:67] op_sel_hi:[1,0,1]
	v_pk_fma_f32 v[64:65], v[12:13], s[66:67], v[68:69] op_sel_hi:[1,0,1]
	v_pk_fma_f32 v[66:67], v[10:11], s[66:67], v[70:71] op_sel_hi:[1,0,1]
	v_pk_fma_f32 v[22:23], v[12:13], s[68:69], v[22:23] op_sel_hi:[1,0,1]
	v_pk_fma_f32 v[24:25], v[10:11], s[68:69], v[24:25] op_sel_hi:[1,0,1]
	v_pk_fma_f32 v[26:27], v[12:13], s[70:71], v[26:27] op_sel_hi:[1,0,1]
	v_pk_fma_f32 v[28:29], v[10:11], s[70:71], v[28:29] op_sel_hi:[1,0,1]
	v_pk_fma_f32 v[30:31], v[12:13], s[94:95], v[30:31] op_sel_hi:[1,0,1]
	v_pk_fma_f32 v[32:33], v[10:11], s[94:95], v[32:33] op_sel_hi:[1,0,1]
	v_pk_fma_f32 v[12:13], v[12:13], s[96:97], v[34:35] op_sel_hi:[1,0,1]
	v_pk_fma_f32 v[10:11], v[10:11], s[96:97], v[36:37] op_sel_hi:[1,0,1]
	s_waitcnt vmcnt(3)
; DI float rdlane(float v, int l) { return __uint_as_float((unsigned)__builtin_amdgcn_readlane((int)__float_as_uint(v), l)); }
; DI void ph_adaln(const float* cnd, const float* cctx, const float* ada_w, float* modp, int gw, int NGW, int lane) {
;     ...
;             for (int kk = 0; kk < 64; ++kk) {
;                 const f32x4 w = __builtin_nontemporal_load((const f32x4*)(wp + (size_t)(hh * 64 + kk) * NMOD));
; #pragma unroll
;                 for (int r = 0; r < 9; ++r) { const float s = rdlane(sv[r][hh], kk); acc[r] += w * s; }
	v_pk_fma_f32 v[34:35], v[16:17], s[10:11], v[44:45] op_sel_hi:[1,0,1]
	v_pk_fma_f32 v[36:37], v[14:15], s[10:11], v[48:49] op_sel_hi:[1,0,1]
	v_pk_fma_f32 v[44:45], v[16:17], s[84:85], v[54:55] op_sel_hi:[1,0,1]
	v_pk_fma_f32 v[48:49], v[14:15], s[84:85], v[62:63] op_sel_hi:[1,0,1]
	v_pk_fma_f32 v[46:47], v[16:17], s[34:35], v[46:47] op_sel_hi:[1,0,1]
	v_pk_fma_f32 v[54:55], v[14:15], s[34:35], v[56:57] op_sel_hi:[1,0,1]
	v_pk_fma_f32 v[56:57], v[16:17], s[4:5], v[58:59] op_sel_hi:[1,0,1]
	v_pk_fma_f32 v[58:59], v[14:15], s[4:5], v[60:61] op_sel_hi:[1,0,1]
	v_pk_fma_f32 v[60:61], v[16:17], s[8:9], v[64:65] op_sel_hi:[1,0,1]
	v_pk_fma_f32 v[62:63], v[14:15], s[8:9], v[66:67] op_sel_hi:[1,0,1]
	v_pk_fma_f32 v[22:23], v[16:17], s[58:59], v[22:23] op_sel_hi:[1,0,1]
	v_pk_fma_f32 v[24:25], v[14:15], s[58:59], v[24:25] op_sel_hi:[1,0,1]
	v_pk_fma_f32 v[26:27], v[16:17], s[60:61], v[26:27] op_sel_hi:[1,0,1]
	v_pk_fma_f32 v[28:29], v[14:15], s[60:61], v[28:29] op_sel_hi:[1,0,1]
	v_pk_fma_f32 v[30:31], v[16:17], s[12:13], v[30:31] op_sel_hi:[1,0,1]
	v_pk_fma_f32 v[32:33], v[14:15], s[12:13], v[32:33] op_sel_hi:[1,0,1]
	v_pk_fma_f32 v[12:13], v[16:17], s[74:75], v[12:13] op_sel_hi:[1,0,1]
	v_pk_fma_f32 v[10:11], v[14:15], s[74:75], v[10:11] op_sel_hi:[1,0,1]
	v_readlane_b32 s72, v76, s37
	v_readlane_b32 s6, v77, s37
	v_readlane_b32 s16, v78, s37
	v_readlane_b32 s18, v79, s37
	v_readlane_b32 s78, v81, s37
	v_readlane_b32 s20, v82, s37
	s_waitcnt vmcnt(2)
	v_pk_fma_f32 v[14:15], v[8:9], s[76:77], v[34:35] op_sel_hi:[1,0,1]
	v_pk_fma_f32 v[16:17], v[6:7], s[76:77], v[36:37] op_sel_hi:[1,0,1]
	v_pk_fma_f32 v[34:35], v[8:9], s[0:1], v[44:45] op_sel_hi:[1,0,1]
	v_pk_fma_f32 v[36:37], v[6:7], s[0:1], v[48:49] op_sel_hi:[1,0,1]
	v_pk_fma_f32 v[44:45], v[8:9], s[2:3], v[46:47] op_sel_hi:[1,0,1]
	v_pk_fma_f32 v[46:47], v[6:7], s[2:3], v[54:55] op_sel_hi:[1,0,1]
	v_pk_fma_f32 v[48:49], v[8:9], s[24:25], v[56:57] op_sel_hi:[1,0,1]
	v_pk_fma_f32 v[54:55], v[6:7], s[24:25], v[58:59] op_sel_hi:[1,0,1]
	v_pk_fma_f32 v[56:57], v[8:9], s[26:27], v[60:61] op_sel_hi:[1,0,1]
	v_pk_fma_f32 v[58:59], v[6:7], s[26:27], v[62:63] op_sel_hi:[1,0,1]
	v_pk_fma_f32 v[22:23], v[8:9], s[56:57], v[22:23] op_sel_hi:[1,0,1]
	v_pk_fma_f32 v[24:25], v[6:7], s[56:57], v[24:25] op_sel_hi:[1,0,1]
	v_pk_fma_f32 v[26:27], v[8:9], s[44:45], v[26:27] op_sel_hi:[1,0,1]
	v_pk_fma_f32 v[28:29], v[6:7], s[44:45], v[28:29] op_sel_hi:[1,0,1]
	v_pk_fma_f32 v[30:31], v[8:9], s[46:47], v[30:31] op_sel_hi:[1,0,1]
	v_pk_fma_f32 v[32:33], v[6:7], s[46:47], v[32:33] op_sel_hi:[1,0,1]
	v_pk_fma_f32 v[8:9], v[8:9], s[50:51], v[12:13] op_sel_hi:[1,0,1]
	v_pk_fma_f32 v[6:7], v[6:7], s[50:51], v[10:11] op_sel_hi:[1,0,1]
	v_readlane_b32 s22, v50, s41
	v_readlane_b32 s48, v74, s41
	v_readlane_b32 s30, v75, s41
	v_readlane_b32 s36, v76, s41
	v_readlane_b32 s38, v77, s41
	v_readlane_b32 s40, v78, s41
	v_readlane_b32 s42, v79, s41
	v_readlane_b32 s28, v81, s41
	v_readlane_b32 s62, v82, s41
	s_waitcnt vmcnt(1)
	v_pk_fma_f32 v[10:11], v[20:21], s[52:53], v[14:15] op_sel_hi:[1,0,1]
	v_pk_fma_f32 v[12:13], v[18:19], s[52:53], v[16:17] op_sel_hi:[1,0,1]
	v_pk_fma_f32 v[14:15], v[20:21], s[54:55], v[34:35] op_sel_hi:[1,0,1]
	v_pk_fma_f32 v[16:17], v[18:19], s[54:55], v[36:37] op_sel_hi:[1,0,1]
	v_pk_fma_f32 v[34:35], v[20:21], s[64:65], v[44:45] op_sel_hi:[1,0,1]
	v_pk_fma_f32 v[36:37], v[18:19], s[64:65], v[46:47] op_sel_hi:[1,0,1]
	v_pk_fma_f32 v[44:45], v[20:21], s[72:73], v[48:49] op_sel_hi:[1,0,1]
	v_pk_fma_f32 v[46:47], v[18:19], s[72:73], v[54:55] op_sel_hi:[1,0,1]
	v_pk_fma_f32 v[48:49], v[20:21], s[6:7], v[56:57] op_sel_hi:[1,0,1]
	v_pk_fma_f32 v[54:55], v[18:19], s[6:7], v[58:59] op_sel_hi:[1,0,1]
	v_pk_fma_f32 v[22:23], v[20:21], s[16:17], v[22:23] op_sel_hi:[1,0,1]
	v_pk_fma_f32 v[24:25], v[18:19], s[16:17], v[24:25] op_sel_hi:[1,0,1]
	v_pk_fma_f32 v[26:27], v[20:21], s[18:19], v[26:27] op_sel_hi:[1,0,1]
	v_pk_fma_f32 v[28:29], v[18:19], s[18:19], v[28:29] op_sel_hi:[1,0,1]
	v_pk_fma_f32 v[30:31], v[20:21], s[78:79], v[30:31] op_sel_hi:[1,0,1]
	v_pk_fma_f32 v[32:33], v[18:19], s[78:79], v[32:33] op_sel_hi:[1,0,1]
	v_pk_fma_f32 v[8:9], v[20:21], s[20:21], v[8:9] op_sel_hi:[1,0,1]
	v_pk_fma_f32 v[6:7], v[18:19], s[20:21], v[6:7] op_sel_hi:[1,0,1]
	v_readlane_b32 s66, v50, s39
	v_readlane_b32 s68, v74, s39
	v_readlane_b32 s70, v75, s39
	v_readlane_b32 s86, v76, s39
	v_readlane_b32 s88, v77, s39
	v_readlane_b32 s10, v78, s39
	v_readlane_b32 s84, v79, s39
	v_readlane_b32 s34, v81, s39
	v_readlane_b32 s90, v82, s39
	s_waitcnt vmcnt(0)
; DI float rdlane(float v, int l) { return __uint_as_float((unsigned)__builtin_amdgcn_readlane((int)__float_as_uint(v), l)); }
; DI void ph_adaln(const float* cnd, const float* cctx, const float* ada_w, float* modp, int gw, int NGW, int lane) {
;     ...
;                 for (int r = 0; r < 9; ++r) { const float s = rdlane(sv[r][hh], kk); acc[r] += w * s; }
;             }
;         }
; #pragma unroll
;         for (int r = 0; r < 9; ++r) *(f32x4*)(modp + ((size_t)((ks * 2 + l) * 9 + r)) * NMOD + col0) = acc[r];
	v_pk_fma_f32 v[10:11], v[4:5], s[22:23], v[10:11] op_sel_hi:[1,0,1]
	v_pk_fma_f32 v[12:13], v[2:3], s[22:23], v[12:13] op_sel_hi:[1,0,1]
	v_pk_fma_f32 v[14:15], v[4:5], s[48:49], v[14:15] op_sel_hi:[1,0,1]
	v_pk_fma_f32 v[16:17], v[2:3], s[48:49], v[16:17] op_sel_hi:[1,0,1]
	v_pk_fma_f32 v[18:19], v[4:5], s[30:31], v[34:35] op_sel_hi:[1,0,1]
	v_pk_fma_f32 v[20:21], v[2:3], s[30:31], v[36:37] op_sel_hi:[1,0,1]
	v_pk_fma_f32 v[44:45], v[4:5], s[36:37], v[44:45] op_sel_hi:[1,0,1]
	v_pk_fma_f32 v[46:47], v[2:3], s[36:37], v[46:47] op_sel_hi:[1,0,1]
	v_pk_fma_f32 v[48:49], v[4:5], s[38:39], v[48:49] op_sel_hi:[1,0,1]
	v_pk_fma_f32 v[54:55], v[2:3], s[38:39], v[54:55] op_sel_hi:[1,0,1]
	v_pk_fma_f32 v[56:57], v[4:5], s[40:41], v[22:23] op_sel_hi:[1,0,1]
	v_pk_fma_f32 v[58:59], v[2:3], s[40:41], v[24:25] op_sel_hi:[1,0,1]
	v_pk_fma_f32 v[60:61], v[4:5], s[42:43], v[26:27] op_sel_hi:[1,0,1]
	v_pk_fma_f32 v[62:63], v[2:3], s[42:43], v[28:29] op_sel_hi:[1,0,1]
	v_pk_fma_f32 v[64:65], v[4:5], s[28:29], v[30:31] op_sel_hi:[1,0,1]
	v_pk_fma_f32 v[66:67], v[2:3], s[28:29], v[32:33] op_sel_hi:[1,0,1]
	v_pk_fma_f32 v[4:5], v[4:5], s[62:63], v[8:9] op_sel_hi:[1,0,1]
	v_pk_fma_f32 v[2:3], v[2:3], s[62:63], v[6:7] op_sel_hi:[1,0,1]
	v_pk_fma_f32 v[36:37], v[40:41], s[66:67], v[10:11] op_sel_hi:[1,0,1]
	v_pk_fma_f32 v[34:35], v[38:39], s[66:67], v[12:13] op_sel_hi:[1,0,1]
	v_pk_fma_f32 v[32:33], v[40:41], s[68:69], v[14:15] op_sel_hi:[1,0,1]
	v_pk_fma_f32 v[30:31], v[38:39], s[68:69], v[16:17] op_sel_hi:[1,0,1]
	v_pk_fma_f32 v[28:29], v[40:41], s[70:71], v[18:19] op_sel_hi:[1,0,1]
	v_pk_fma_f32 v[26:27], v[38:39], s[70:71], v[20:21] op_sel_hi:[1,0,1]
	v_pk_fma_f32 v[24:25], v[40:41], s[86:87], v[44:45] op_sel_hi:[1,0,1]
	v_pk_fma_f32 v[22:23], v[38:39], s[86:87], v[46:47] op_sel_hi:[1,0,1]
	v_pk_fma_f32 v[20:21], v[40:41], s[88:89], v[48:49] op_sel_hi:[1,0,1]
	v_pk_fma_f32 v[18:19], v[38:39], s[88:89], v[54:55] op_sel_hi:[1,0,1]
	v_pk_fma_f32 v[16:17], v[40:41], s[10:11], v[56:57] op_sel_hi:[1,0,1]
	v_pk_fma_f32 v[14:15], v[38:39], s[10:11], v[58:59] op_sel_hi:[1,0,1]
	v_pk_fma_f32 v[12:13], v[40:41], s[84:85], v[60:61] op_sel_hi:[1,0,1]
	v_pk_fma_f32 v[10:11], v[38:39], s[84:85], v[62:63] op_sel_hi:[1,0,1]
	v_pk_fma_f32 v[8:9], v[40:41], s[34:35], v[64:65] op_sel_hi:[1,0,1]
	v_pk_fma_f32 v[6:7], v[38:39], s[34:35], v[66:67] op_sel_hi:[1,0,1]
	v_pk_fma_f32 v[4:5], v[40:41], s[90:91], v[4:5] op_sel_hi:[1,0,1]
	v_pk_fma_f32 v[2:3], v[38:39], s[90:91], v[2:3] op_sel_hi:[1,0,1]
	s_cbranch_scc1 .LBB0_11
	s_lshl_b32 s0, s29, 1
	v_readlane_b32 s6, v251, 26
	s_add_i32 s0, s0, s31
	v_readlane_b32 s7, v251, 27
	s_mul_i32 s0, s0, 9
	s_add_i32 s2, s0, 1
	v_lshl_add_u64 v[38:39], v[52:53], 2, s[6:7]
	v_mad_i64_i32 v[40:41], s[6:7], s0, v80, v[38:39]
	global_store_dwordx4 v[40:41], v[34:37], off sc1
	s_load_dwordx16 s[36:51], s[82:83], 0x0
	s_add_i32 s1, s1, s80
	v_mad_i64_i32 v[34:35], s[6:7], s2, v80, v[38:39]
	s_add_i32 s2, s0, 2
	global_store_dwordx4 v[34:35], v[30:33], off sc1
	s_sub_i32 s5, s5, s80
	s_mov_b32 s78, s80
	v_mad_i64_i32 v[30:31], s[6:7], s2, v80, v[38:39]
	s_add_i32 s2, s0, 3
	global_store_dwordx4 v[30:31], v[26:29], off sc1
	s_mov_b64 s[62:63], s[82:83]
	s_nop 0
	v_mad_i64_i32 v[26:27], s[6:7], s2, v80, v[38:39]
	s_add_i32 s2, s0, 4
	global_store_dwordx4 v[26:27], v[22:25], off sc1
	s_nop 1
	v_mad_i64_i32 v[22:23], s[6:7], s2, v80, v[38:39]
	s_add_i32 s2, s0, 5
	global_store_dwordx4 v[22:23], v[18:21], off sc1
	s_nop 1
	v_mad_i64_i32 v[18:19], s[6:7], s2, v80, v[38:39]
	s_add_i32 s2, s0, 6
	global_store_dwordx4 v[18:19], v[14:17], off sc1
	s_nop 1
	v_mad_i64_i32 v[14:15], s[6:7], s2, v80, v[38:39]
	s_add_i32 s2, s0, 7
	global_store_dwordx4 v[14:15], v[10:13], off sc1
	s_add_i32 s0, s0, 8
	s_cmpk_gt_i32 s1, 0x5ff
	v_mad_i64_i32 v[10:11], s[6:7], s2, v80, v[38:39]
	global_store_dwordx4 v[10:11], v[6:9], off sc1
	s_nop 1
	v_mad_i64_i32 v[6:7], s[6:7], s0, v80, v[38:39]
	global_store_dwordx4 v[6:7], v[2:5], off sc1
	s_cbranch_scc0 .LBB0_8
	s_load_dwordx4 s[80:83], s[62:63], 0xa0
	s_load_dwordx8 s[52:59], s[62:63], 0x80
	v_readlane_b32 s96, v251, 36
	v_readlane_b32 s4, v251, 38
	s_mov_b32 s2, s3
	v_readlane_b32 s86, v251, 40
	s_mov_b32 s88, s61
	v_readlane_b32 s97, v251, 37
	v_readlane_b32 s5, v251, 39
	v_readlane_b32 s87, v251, 41

; __device__ __forceinline__ unsigned xb_add(unsigned* p, unsigned v) { return __hip_atomic_fetch_add(p, v, __ATOMIC_RELAXED, __HIP_MEMORY_SCOPE_AGENT); }
; __device__ __forceinline__ void xcd_barrier(const XcdBarrier& b) {
;     ...
;             asm volatile("buffer_inv sc1" ::: "memory");
;             __builtin_amdgcn_fence(__ATOMIC_RELEASE, "agent");
;             asm volatile("s_waitcnt vmcnt(0)" ::: "memory");
;             const unsigned og = xb_add(&bar[XB_TOP], 1u);
.LBB0_47:
	s_andn2_saveexec_b64 s[0:1], s[0:1]
	s_cbranch_execz .LBB0_67
	s_mov_b64 s[0:1], exec
	buffer_inv sc1
	s_nop 0
	s_waitcnt vmcnt(0) lgkmcnt(0)
	s_waitcnt vmcnt(0)
	v_mbcnt_lo_u32_b32 v2, s0, 0
	v_mbcnt_hi_u32_b32 v2, s1, v2
	v_cmp_eq_u32_e32 vcc, 0, v2
	s_and_saveexec_b64 s[10:11], vcc
	s_cbranch_execz .LBB0_50
	s_bcnt1_i32_b64 s0, s[0:1]
	v_mov_b32_e32 v3, 0x7000
	v_mov_b32_e32 v4, s0
	global_atomic_add v3, v3, v4, s[82:83] offset:1024 sc0

; DI void ph_modred(const float* modp, const float* ada_b, float* mod, int gtid, int GT) {
;     for (int i = gtid; i < 2 * 9 * NMOD; i += GT) { const int l = i / (9 * NMOD), j = i % NMOD; float s = ada_b[l * NMOD + j];
; #pragma unroll
;         for (int ks = 0; ks < KSPLIT; ++ks) s += modp[(size_t)ks * (2 * 9 * NMOD) + i];
;         mod[i] = s; }
.LBB0_71:
	v_add_co_u32_e32 v6, vcc, s13, v4
	v_mul_hi_i32 v29, v1, s9
	s_nop 0
	v_addc_co_u32_e32 v7, vcc, -1, v5, vcc
	v_add_co_u32_e32 v8, vcc, s14, v4
	v_lshrrev_b32_e32 v32, 31, v29
	s_nop 0
	v_addc_co_u32_e32 v9, vcc, -1, v5, vcc
	v_add_co_u32_e32 v10, vcc, s15, v4
	v_ashrrev_i32_e32 v33, 11, v29
	s_nop 0
	v_addc_co_u32_e32 v11, vcc, -1, v5, vcc
	v_add_co_u32_e32 v12, vcc, s16, v4
	v_mul_hi_i32 v3, v1, s3
	s_nop 0
	v_addc_co_u32_e32 v13, vcc, -1, v5, vcc
	v_add_co_u32_e32 v14, vcc, s17, v4
	global_load_dword v30, v[4:5], off
	s_nop 0
	v_addc_co_u32_e32 v15, vcc, -1, v5, vcc
	v_add_co_u32_e32 v16, vcc, s18, v4
	v_lshrrev_b32_e32 v31, 31, v3
	s_nop 0
	v_addc_co_u32_e32 v17, vcc, -1, v5, vcc
	v_add_co_u32_e32 v18, vcc, s19, v4
	v_ashrrev_i32_e32 v3, 15, v3
	s_nop 0
	v_addc_co_u32_e32 v19, vcc, -1, v5, vcc
	v_add_co_u32_e32 v20, vcc, s20, v4
	v_add_u32_e32 v3, v3, v31
	s_nop 0
	v_addc_co_u32_e32 v21, vcc, 0, v5, vcc
	v_add_co_u32_e32 v22, vcc, s21, v4
	s_nop 1
	v_addc_co_u32_e32 v23, vcc, 0, v5, vcc
	v_add_co_u32_e32 v24, vcc, s22, v4
	s_nop 1
	v_addc_co_u32_e32 v25, vcc, 0, v5, vcc
	v_add_co_u32_e32 v26, vcc, s23, v4
	s_nop 1
	v_addc_co_u32_e32 v27, vcc, 0, v5, vcc
	global_load_dword v34, v[6:7], off
	global_load_dword v35, v[8:9], off
	s_nop 0
	global_load_dword v10, v[10:11], off
	s_nop 0
	global_load_dword v11, v[12:13], off
	s_nop 0
	global_load_dword v12, v[14:15], off
	global_load_dword v13, v[16:17], off
	s_nop 0
	global_load_dword v14, v[18:19], off
	global_load_dword v15, v[20:21], off
	global_load_dword v16, v[22:23], off
	global_load_dword v17, v[24:25], off
	s_nop 0
	global_load_dword v18, v[26:27], off
	v_add_u32_e32 v7, v33, v32
	v_mul_i32_i24_e32 v7, 0x3000, v7
	v_sub_u32_e32 v7, v1, v7
	v_mad_i32_i24 v8, v3, s12, v7
	v_ashrrev_i32_e32 v9, 31, v8
	v_lshl_add_u64 v[8:9], v[8:9], 2, s[54:55]
	global_load_dword v3, v[8:9], off
	v_add_co_u32_e32 v28, vcc, s24, v4
	v_add_u32_e32 v1, s8, v1
	s_nop 0
	v_addc_co_u32_e32 v29, vcc, 0, v5, vcc
	v_add_co_u32_e32 v6, vcc, s25, v4
	s_waitcnt vmcnt(0)
	v_add_f32_e32 v3, v3, v34
	v_addc_co_u32_e32 v7, vcc, 0, v5, vcc
	v_add_co_u32_e32 v8, vcc, s26, v4
	global_load_dword v19, v[28:29], off
	global_load_dword v20, v[6:7], off
	v_addc_co_u32_e32 v9, vcc, 0, v5, vcc
	v_add_co_u32_e32 v6, vcc, 0x6c0000, v4
	v_add_f32_e32 v3, v3, v35
	s_nop 0
	v_addc_co_u32_e32 v7, vcc, 0, v5, vcc
	global_load_dword v8, v[8:9], off
	s_nop 0
	global_load_dword v9, v[6:7], off
	v_add_f32_e32 v3, v3, v10
	v_add_f32_e32 v3, v3, v11
	v_add_f32_e32 v3, v3, v12
	v_add_f32_e32 v3, v3, v13
	v_add_f32_e32 v3, v3, v14
	v_add_f32_e32 v3, v3, v30
	v_add_f32_e32 v3, v3, v15
	v_add_f32_e32 v3, v3, v16
	v_add_f32_e32 v3, v3, v17
	v_add_f32_e32 v3, v3, v18
	v_add_co_u32_e32 v6, vcc, 0xff918000, v4
	s_waitcnt vmcnt(3)
	v_add_f32_e32 v3, v3, v19
	v_addc_co_u32_e32 v7, vcc, -1, v5, vcc
	s_waitcnt vmcnt(2)
	v_add_f32_e32 v3, v3, v20
	v_cmp_lt_i32_e32 vcc, s27, v1
	v_lshl_add_u64 v[4:5], v[4:5], 0, s[6:7]
	s_or_b64 s[10:11], vcc, s[10:11]
	s_waitcnt vmcnt(1)
	v_add_f32_e32 v3, v3, v8
	s_waitcnt vmcnt(0)
	v_add_f32_e32 v3, v3, v9
	global_store_dword v[6:7], v3, off sc1
	s_andn2_b64 exec, exec, s[10:11]
	s_cbranch_execnz .LBB0_71

; DI void ph_rwt(const float* rw, float* rwT, int gtid, int GT) {
;     for (int i = gtid; i < 2 * 16 * DM; i += GT) { const int l = i >> 15, e = (i >> 11) & 15, d = i & (DM - 1); rwT[i] = rw[(size_t)l * DM * 16 + d * 16 + e]; }
.LBB0_74:
	v_ashrrev_i32_e32 v8, 15, v3
	v_ashrrev_i32_e32 v9, 31, v8
	v_and_b32_e32 v6, 0x7ff0, v1
	v_lshlrev_b64 v[8:9], 17, v[8:9]
	v_lshrrev_b32_e32 v10, 9, v3
	v_lshlrev_b32_e32 v6, 2, v6
	v_lshl_add_u64 v[8:9], s[52:53], 0, v[8:9]
	v_lshl_add_u64 v[8:9], v[8:9], 0, v[6:7]
	v_and_b32_e32 v6, 60, v10
	v_lshl_add_u64 v[8:9], v[8:9], 0, v[6:7]
	global_load_dword v6, v[8:9], off
	v_add_u32_e32 v3, s8, v3
	v_cmp_lt_i32_e32 vcc, s9, v3
	v_add_u32_e32 v1, s3, v1
	s_or_b64 s[10:11], vcc, s[10:11]
	s_waitcnt vmcnt(0)
	global_store_dword v[4:5], v6, off sc1
	v_lshl_add_u64 v[4:5], v[4:5], 0, s[6:7]
	s_andn2_b64 exec, exec, s[10:11]
	s_cbranch_execnz .LBB0_74

; #define PHASE(k) if (IN(k)) _Pragma("unroll") for (int rep_ = 0; rep_ < 1 + (int)((DUP_MASK >> (k)) & 1u); ++rep_)
; #define REP_BAR() do { if (rep_) GRID_BAR(); } while (0)
; __global__ void __launch_bounds__(512, 2) dit_fwd(Args args) {
;     ...
;     PHASE(1) { REP_BAR(); ph_modred(modp, ada_b, mod, bid * 512 + tid, G * 512); ph_rwt(router_w, rwt, bid * 512 + tid, G * 512); for (int i = bid * 512 + tid; i < YT; i += G * 512) idmap[i] = i; } SEAM(1);
.LBB0_78:
	v_ashrrev_i32_e32 v13, 31, v4
	v_mov_b32_e32 v12, v4
	v_add_u32_e32 v8, -2, v8
	v_ashrrev_i32_e32 v11, 31, v5
	v_mov_b32_e32 v10, v5
	v_lshl_add_u64 v[12:13], v[12:13], 2, s[12:13]
	v_cmp_eq_u32_e32 vcc, 0, v8
	v_add_u32_e32 v3, s8, v7
	v_add_u32_e32 v5, s9, v5
	v_add_u32_e32 v4, s3, v4
	v_lshl_add_u64 v[10:11], v[10:11], 2, s[12:13]
	global_store_dword v[12:13], v7, off sc1
	global_store_dword v[10:11], v3, off sc1
	s_or_b64 s[10:11], vcc, s[10:11]
	v_add_u32_e32 v7, s3, v7
	s_andn2_b64 exec, exec, s[10:11]
	s_cbranch_execnz .LBB0_78
	s_or_b64 exec, exec, s[10:11]
	v_mad_u64_u32 v[2:3], s[10:11], v6, s8, v[2:3]
	v_cmp_ne_u32_e32 vcc, v1, v6
	s_orn2_b64 s[10:11], vcc, exec

; #define PHASE(k) if (IN(k)) _Pragma("unroll") for (int rep_ = 0; rep_ < 1 + (int)((DUP_MASK >> (k)) & 1u); ++rep_)
; #define REP_BAR() do { if (rep_) GRID_BAR(); } while (0)
; __global__ void __launch_bounds__(512, 2) dit_fwd(Args args) {
;     ...
;     PHASE(1) { REP_BAR(); ph_modred(modp, ada_b, mod, bid * 512 + tid, G * 512); ph_rwt(router_w, rwt, bid * 512 + tid, G * 512); for (int i = bid * 512 + tid; i < YT; i += G * 512) idmap[i] = i; } SEAM(1);
.LBB0_82:
	global_store_dword v[4:5], v2, off sc1
	v_add_u32_e32 v2, s8, v2
	v_cmp_lt_i32_e32 vcc, s3, v2
	s_or_b64 s[10:11], vcc, s[10:11]
	v_lshl_add_u64 v[4:5], v[4:5], 0, s[6:7]
	s_andn2_b64 exec, exec, s[10:11]
	s_cbranch_execnz .LBB0_82

; __device__ __forceinline__ unsigned xb_add(unsigned* p, unsigned v) { return __hip_atomic_fetch_add(p, v, __ATOMIC_RELAXED, __HIP_MEMORY_SCOPE_AGENT); }
; __device__ __forceinline__ void xcd_barrier(const XcdBarrier& b) {
;     ...
;             asm volatile("buffer_inv sc1" ::: "memory");
;             __builtin_amdgcn_fence(__ATOMIC_RELEASE, "agent");
;             asm volatile("s_waitcnt vmcnt(0)" ::: "memory");
;             const unsigned og = xb_add(&bar[XB_TOP], 1u);
.LBB0_117:
	s_andn2_saveexec_b64 s[8:9], s[8:9]
	s_cbranch_execz .LBB0_137
	s_mov_b64 s[8:9], exec
	buffer_inv sc1
	s_nop 0
	s_waitcnt vmcnt(0) lgkmcnt(0)
	s_waitcnt vmcnt(0)
	v_mbcnt_lo_u32_b32 v2, s8, 0
	v_mbcnt_hi_u32_b32 v2, s9, v2
	v_cmp_eq_u32_e32 vcc, 0, v2
	s_and_saveexec_b64 s[10:11], vcc
	s_cbranch_execz .LBB0_120
	s_bcnt1_i32_b64 s3, s[8:9]
	v_mov_b32_e32 v3, 0x7000
	v_mov_b32_e32 v4, s3
	global_atomic_add v3, v3, v4, s[82:83] offset:1024 sc0
